# baseline (speedup 1.0000x reference)
.LBB1_2:
	v_or_b32_e32 v118, 0x14000, v1
	v_mov_b32_e32 v99, 0
	s_bfe_u32 s40, s19, 0x20006
	s_waitcnt vmcnt(4)
	s_barrier
	s_mov_b64 s[20:21], 0x80
	s_add_u32 s58, s2, s20
	s_addc_u32 s59, s3, s21
	v_readfirstlane_b32 s19, v118
	s_mov_b32 m0, s19
	v_or_b32_e32 v119, 0x16000, v1
	global_load_lds_dwordx4 v100, s[58:59]
	v_readfirstlane_b32 s19, v119
	s_add_u32 s58, s2, s20
	s_addc_u32 s59, s3, s21
	s_mov_b32 m0, s19
	v_or_b32_e32 v120, 0x6000, v1
	global_load_lds_dwordx4 v103, s[58:59]
	v_readfirstlane_b32 s19, v120
	s_add_u32 s58, s16, s20
	s_addc_u32 s59, s17, s21
	v_or_b32_e32 v3, 0x8000, v1
	s_mov_b32 m0, s19
	v_cndmask_b32_e32 v121, v2, v3, vcc
	global_load_lds_dwordx4 v100, s[58:59]
	v_readfirstlane_b32 s19, v121
	s_add_u32 s58, s16, s20
	s_addc_u32 s59, s17, s21
	v_or_b32_e32 v123, 0x18000, v1
	s_mov_b32 m0, s19
	s_add_u32 s20, s2, 0x40080
	v_mov_b32_e32 v3, v100
	v_readfirstlane_b32 s22, v123
	v_or_b32_e32 v124, 0x1a000, v1
	global_load_lds_dwordx4 v101, s[58:59]
	s_addc_u32 s21, s3, 0
	s_mov_b32 m0, s22
	v_readfirstlane_b32 s22, v124
	global_load_lds_dwordx4 v3, s[20:21]
	v_mov_b32_e32 v3, v103
	s_mov_b32 m0, s22
	v_lshlrev_b32_e32 v4, 6, v0
	global_load_lds_dwordx4 v3, s[20:21]
	v_and_b32_e32 v105, 15, v0
	v_and_b32_e32 v3, 48, v0
	v_and_b32_e32 v4, 0x3c0, v4
	v_lshlrev_b32_e32 v6, 2, v0
	s_mul_i32 s37, s18, 48
	s_mov_b32 s1, 0x14000
	s_mov_b32 s19, 0x18000
	s_waitcnt vmcnt(6)
	v_or_b32_e32 v5, v4, v3
	v_and_b32_e32 v6, 32, v6
	v_lshlrev_b32_e32 v10, 6, v105
	s_add_i32 s39, s37, 16
	s_add_i32 s38, s37, 32
	s_lshl_b32 s26, s40, 12
	v_bitop3_b32 v4, v4, v6, v3 bitop3:0x36
	v_add_u32_e32 v7, 0xb000, v1
	v_bitop3_b32 v8, v5, s0, v6 bitop3:0xde
	v_bitop3_b32 v9, v5, s1, v6 bitop3:0xde
	v_bitop3_b32 v5, v5, s19, v6 bitop3:0xde
	v_bitop3_b32 v3, v10, v6, v3 bitop3:0x36
	s_mulk_i32 s18, 0x1800
	s_lshl_b32 s19, s39, 7
	s_lshl_b32 s20, s38, 7
	v_lshrrev_b32_e32 v102, 2, v0
	v_cndmask_b32_e32 v125, v2, v7, vcc
	s_mov_b32 s41, -2
	s_mov_b64 s[0:1], 0
	v_add_u32_e32 v126, s26, v4
	v_add_u32_e32 v110, s18, v3
	v_add_u32_e32 v109, s19, v4
	v_add_u32_e32 v108, s20, v4
	s_mov_b64 s[18:19], 0x30080
	v_add_u32_e32 v127, 0x9000, v1
	v_add_u32_e32 v122, s26, v8
	s_mov_b64 s[20:21], 0x100
	s_mov_b64 s[22:23], 0x40100
	v_add_u32_e32 v117, s26, v9
	s_mov_b64 s[24:25], 0x30100
	v_add_u32_e32 v114, s26, v5
	s_mov_b64 s[26:27], 0x180
	s_mov_b64 s[28:29], 0x40180
	v_mov_b32_e32 v2, v99
	v_mov_b32_e32 v3, v99
	v_mov_b32_e32 v4, v99
	v_mov_b32_e32 v5, v99
	v_mov_b32_e32 v6, v99
	v_mov_b32_e32 v7, v99
	v_mov_b32_e32 v8, v99
	v_mov_b32_e32 v9, v99
	v_mov_b32_e32 v10, v99
	v_mov_b32_e32 v11, v99
	v_mov_b32_e32 v12, v99
	v_mov_b32_e32 v13, v99
	v_mov_b32_e32 v14, v99
	v_mov_b32_e32 v15, v99
	v_mov_b32_e32 v16, v99
	v_mov_b32_e32 v17, v99
	v_mov_b32_e32 v18, v99
	v_mov_b32_e32 v19, v99
	v_mov_b32_e32 v20, v99
	v_mov_b32_e32 v21, v99
	v_mov_b32_e32 v22, v99
	v_mov_b32_e32 v23, v99
	v_mov_b32_e32 v24, v99
	v_mov_b32_e32 v25, v99
	v_mov_b32_e32 v26, v99
	v_mov_b32_e32 v27, v99
	v_mov_b32_e32 v28, v99
	v_mov_b32_e32 v29, v99
	v_mov_b32_e32 v30, v99
	v_mov_b32_e32 v31, v99
	v_mov_b32_e32 v32, v99
	v_mov_b32_e32 v33, v99
	v_mov_b32_e32 v34, v99
	v_mov_b32_e32 v35, v99
	v_mov_b32_e32 v36, v99
	v_mov_b32_e32 v37, v99
	v_mov_b32_e32 v38, v99
	v_mov_b32_e32 v39, v99
	v_mov_b32_e32 v40, v99
	v_mov_b32_e32 v41, v99
	v_mov_b32_e32 v42, v99
	v_mov_b32_e32 v43, v99
	v_mov_b32_e32 v44, v99
	v_mov_b32_e32 v45, v99
	v_mov_b32_e32 v46, v99
	v_mov_b32_e32 v47, v99
	v_mov_b32_e32 v48, v99
	v_mov_b32_e32 v49, v99
	v_mov_b32_e32 v50, v99
	v_mov_b32_e32 v51, v99
	v_mov_b32_e32 v52, v99
	v_mov_b32_e32 v53, v99
	v_mov_b32_e32 v62, v99
	v_mov_b32_e32 v63, v99
	v_mov_b32_e32 v64, v99
	v_mov_b32_e32 v65, v99
	v_mov_b32_e32 v66, v99
	v_mov_b32_e32 v67, v99
	v_mov_b32_e32 v68, v99
	v_mov_b32_e32 v69, v99
	v_mov_b32_e32 v70, v99
	v_mov_b32_e32 v71, v99
	v_mov_b32_e32 v72, v99
	v_mov_b32_e32 v73, v99
	v_mov_b32_e32 v74, v99
	v_mov_b32_e32 v75, v99
	v_mov_b32_e32 v76, v99
	v_mov_b32_e32 v77, v99
	v_mov_b32_e32 v78, v99
	v_mov_b32_e32 v79, v99
	v_mov_b32_e32 v80, v99
	v_mov_b32_e32 v81, v99
	v_mov_b32_e32 v82, v99
	v_mov_b32_e32 v83, v99
	v_mov_b32_e32 v84, v99
	v_mov_b32_e32 v85, v99
	v_mov_b32_e32 v86, v99
	v_mov_b32_e32 v87, v99
	v_mov_b32_e32 v88, v99
	v_mov_b32_e32 v89, v99
	v_mov_b32_e32 v90, v99
	v_mov_b32_e32 v91, v99
	v_mov_b32_e32 v92, v99
	v_mov_b32_e32 v93, v99
	v_mov_b32_e32 v94, v99
	v_mov_b32_e32 v95, v99
	v_mov_b32_e32 v96, v99
	v_mov_b32_e32 v97, v99
	v_mov_b32_e32 v54, v99
	v_mov_b32_e32 v55, v99
	v_mov_b32_e32 v56, v99
	v_mov_b32_e32 v57, v99
	v_mov_b32_e32 v58, v99
	v_mov_b32_e32 v59, v99
	v_mov_b32_e32 v60, v99
	v_mov_b32_e32 v61, v99
	s_barrier
	v_readfirstlane_b32 s60, v127
	v_readfirstlane_b32 s61, v125
	v_readfirstlane_b32 s62, v106
	v_readfirstlane_b32 s63, v107
	v_readfirstlane_b32 s64, v1
	v_readfirstlane_b32 s65, v111
	v_readfirstlane_b32 s66, v112
	v_readfirstlane_b32 s67, v113
	v_readfirstlane_b32 s68, v115
	v_readfirstlane_b32 s69, v116
	v_readfirstlane_b32 s70, v118
	v_readfirstlane_b32 s71, v119
	v_readfirstlane_b32 s72, v120
	v_readfirstlane_b32 s73, v121
	v_readfirstlane_b32 s74, v123
	v_readfirstlane_b32 s75, v124
.LBB1_3:
	ds_read_b128 v[128:131], v126 offset:49152
	ds_read_b128 v[132:135], v126 offset:50176
	ds_read_b128 v[136:139], v126 offset:51200
	ds_read_b128 v[140:143], v126 offset:52224
	s_add_u32 s30, s16, s0
	s_addc_u32 s31, s17, s1
	ds_read_b128 v[144:147], v110
	ds_read_b128 v[148:151], v110 offset:1024
	ds_read_b128 v[152:155], v109
	ds_read_b128 v[156:159], v109 offset:1024
	ds_read_b128 v[160:163], v108
	ds_read_b128 v[164:167], v108 offset:1024
	s_mov_b32 s34, s60
	s_add_u32 s52, s30, s18
	s_addc_u32 s53, s31, s19
	s_mov_b32 m0, s34
	s_nop 0
	global_load_lds_dwordx4 v100, s[52:53]
	s_mov_b32 s34, s61
	s_add_u32 s52, s30, s18
	s_addc_u32 s53, s31, s19
	s_mov_b32 m0, s34
	s_nop 0
	global_load_lds_dwordx4 v101, s[52:53]
	s_waitcnt lgkmcnt(6)
	s_barrier
	s_waitcnt lgkmcnt(0)
	s_setprio 1
	s_waitcnt lgkmcnt(0)
	v_mfma_f32_16x16x32_f16 v[94:97], v[144:147], v[128:131], v[94:97]
	v_mfma_f32_16x16x32_f16 v[90:93], v[144:147], v[136:139], v[90:93]
	v_mfma_f32_16x16x32_f16 v[86:89], v[152:155], v[128:131], v[86:89]
	v_mfma_f32_16x16x32_f16 v[82:85], v[152:155], v[136:139], v[82:85]
	v_mfma_f32_16x16x32_f16 v[78:81], v[160:163], v[128:131], v[78:81]
	v_mfma_f32_16x16x32_f16 v[74:77], v[160:163], v[136:139], v[74:77]
	v_mfma_f32_16x16x32_f16 v[94:97], v[148:151], v[132:135], v[94:97]
	v_mfma_f32_16x16x32_f16 v[90:93], v[148:151], v[140:143], v[90:93]
	v_mfma_f32_16x16x32_f16 v[86:89], v[156:159], v[132:135], v[86:89]
	v_mfma_f32_16x16x32_f16 v[82:85], v[156:159], v[140:143], v[82:85]
	v_mfma_f32_16x16x32_f16 v[78:81], v[164:167], v[132:135], v[78:81]
	v_mfma_f32_16x16x32_f16 v[74:77], v[164:167], v[140:143], v[74:77]
	s_setprio 0
	s_barrier
	s_add_u32 s34, s2, s0
	s_addc_u32 s35, s3, s1
	ds_read_b128 v[168:171], v122
	ds_read_b128 v[172:175], v122 offset:1024
	ds_read_b128 v[176:179], v122 offset:2048
	ds_read_b128 v[180:183], v122 offset:3072
	s_mov_b32 s42, s62
	s_add_u32 s54, s34, s20
	s_addc_u32 s55, s35, s21
	s_mov_b32 m0, s42
	s_nop 0
	global_load_lds_dwordx4 v100, s[54:55]
	s_mov_b32 s42, s63
	s_add_u32 s54, s34, s20
	s_addc_u32 s55, s35, s21
	s_mov_b32 m0, s42
	s_nop 0
	global_load_lds_dwordx4 v103, s[54:55]
	s_barrier
	s_waitcnt lgkmcnt(0)
	s_setprio 1
	s_waitcnt lgkmcnt(0)
	v_mfma_f32_16x16x32_f16 v[70:73], v[144:147], v[168:171], v[70:73]
	v_mfma_f32_16x16x32_f16 v[66:69], v[144:147], v[176:179], v[66:69]
	v_mfma_f32_16x16x32_f16 v[62:65], v[152:155], v[168:171], v[62:65]
	v_mfma_f32_16x16x32_f16 v[50:53], v[152:155], v[176:179], v[50:53]
	v_mfma_f32_16x16x32_f16 v[46:49], v[160:163], v[168:171], v[46:49]
	v_mfma_f32_16x16x32_f16 v[42:45], v[160:163], v[176:179], v[42:45]
	v_mfma_f32_16x16x32_f16 v[70:73], v[148:151], v[172:175], v[70:73]
	v_mfma_f32_16x16x32_f16 v[66:69], v[148:151], v[180:183], v[66:69]
	v_mfma_f32_16x16x32_f16 v[62:65], v[156:159], v[172:175], v[62:65]
	v_mfma_f32_16x16x32_f16 v[50:53], v[156:159], v[180:183], v[50:53]
	v_mfma_f32_16x16x32_f16 v[46:49], v[164:167], v[172:175], v[46:49]
	v_mfma_f32_16x16x32_f16 v[42:45], v[164:167], v[180:183], v[42:45]
	s_setprio 0
	s_barrier
	ds_read_b128 v[144:147], v110 offset:12288
	ds_read_b128 v[148:151], v110 offset:13312
	ds_read_b128 v[152:155], v109 offset:12288
	ds_read_b128 v[156:159], v109 offset:13312
	ds_read_b128 v[160:163], v108 offset:12288
	ds_read_b128 v[164:167], v108 offset:13312
	s_mov_b32 s42, s64
	s_add_u32 s54, s30, s20
	s_addc_u32 s55, s31, s21
	s_mov_b32 m0, s42
	s_nop 0
	global_load_lds_dwordx4 v100, s[54:55]
	s_mov_b32 s42, s65
	s_add_u32 s54, s30, s20
	s_addc_u32 s55, s31, s21
	s_mov_b32 m0, s42
	s_nop 0
	global_load_lds_dwordx4 v101, s[54:55]
	s_barrier
	s_waitcnt lgkmcnt(0)
	s_setprio 1
	s_waitcnt lgkmcnt(0)
	v_mfma_f32_16x16x32_f16 v[38:41], v[144:147], v[128:131], v[38:41]
	v_mfma_f32_16x16x32_f16 v[34:37], v[144:147], v[136:139], v[34:37]
	v_mfma_f32_16x16x32_f16 v[30:33], v[152:155], v[128:131], v[30:33]
	v_mfma_f32_16x16x32_f16 v[26:29], v[152:155], v[136:139], v[26:29]
	v_mfma_f32_16x16x32_f16 v[22:25], v[160:163], v[128:131], v[22:25]
	v_mfma_f32_16x16x32_f16 v[18:21], v[160:163], v[136:139], v[18:21]
	v_mfma_f32_16x16x32_f16 v[38:41], v[148:151], v[132:135], v[38:41]
	v_mfma_f32_16x16x32_f16 v[34:37], v[148:151], v[140:143], v[34:37]
	v_mfma_f32_16x16x32_f16 v[30:33], v[156:159], v[132:135], v[30:33]
	v_mfma_f32_16x16x32_f16 v[26:29], v[156:159], v[140:143], v[26:29]
	v_mfma_f32_16x16x32_f16 v[22:25], v[164:167], v[132:135], v[22:25]
	v_mfma_f32_16x16x32_f16 v[18:21], v[164:167], v[140:143], v[18:21]
	s_setprio 0
	s_barrier
	s_mov_b32 s42, s66
	s_add_u32 s56, s34, s22
	s_addc_u32 s57, s35, s23
	s_mov_b32 m0, s42
	s_nop 0
	global_load_lds_dwordx4 v100, s[56:57]
	s_mov_b32 s42, s67
	s_add_u32 s56, s34, s22
	s_addc_u32 s57, s35, s23
	s_mov_b32 m0, s42
	s_nop 0
	global_load_lds_dwordx4 v103, s[56:57]
	s_waitcnt vmcnt(6)
	s_barrier
	s_setprio 1
	v_mfma_f32_16x16x32_f16 v[14:17], v[144:147], v[168:171], v[14:17]
	v_mfma_f32_16x16x32_f16 v[10:13], v[144:147], v[176:179], v[10:13]
	v_mfma_f32_16x16x32_f16 v[6:9], v[152:155], v[168:171], v[6:9]
	v_mfma_f32_16x16x32_f16 v[2:5], v[152:155], v[176:179], v[2:5]
	v_mfma_f32_16x16x32_f16 v[54:57], v[160:163], v[168:171], v[54:57]
	v_mfma_f32_16x16x32_f16 v[58:61], v[160:163], v[176:179], v[58:61]
	v_mfma_f32_16x16x32_f16 v[14:17], v[148:151], v[172:175], v[14:17]
	v_mfma_f32_16x16x32_f16 v[10:13], v[148:151], v[180:183], v[10:13]
	v_mfma_f32_16x16x32_f16 v[6:9], v[156:159], v[172:175], v[6:9]
	v_mfma_f32_16x16x32_f16 v[2:5], v[156:159], v[180:183], v[2:5]
	v_mfma_f32_16x16x32_f16 v[54:57], v[164:167], v[172:175], v[54:57]
	v_mfma_f32_16x16x32_f16 v[58:61], v[164:167], v[180:183], v[58:61]
	s_setprio 0
	s_barrier
	ds_read_b128 v[128:131], v117
	ds_read_b128 v[132:135], v117 offset:1024
	ds_read_b128 v[136:139], v117 offset:2048
	ds_read_b128 v[140:143], v117 offset:3072
	ds_read_b128 v[144:147], v110 offset:24576
	ds_read_b128 v[148:151], v110 offset:25600
	ds_read_b128 v[152:155], v109 offset:24576
	ds_read_b128 v[156:159], v109 offset:25600
	ds_read_b128 v[160:163], v108 offset:24576
	ds_read_b128 v[164:167], v108 offset:25600
	s_mov_b32 s42, s68
	s_add_u32 s52, s30, s24
	s_addc_u32 s53, s31, s25
	s_mov_b32 m0, s42
	s_nop 0
	global_load_lds_dwordx4 v100, s[52:53]
	s_mov_b32 s42, s69
	s_add_u32 s52, s30, s24
	s_addc_u32 s53, s31, s25
	s_mov_b32 m0, s42
	s_nop 0
	global_load_lds_dwordx4 v101, s[52:53]
	s_waitcnt lgkmcnt(6)
	s_barrier
	s_waitcnt lgkmcnt(0)
	s_setprio 1
	s_waitcnt lgkmcnt(0)
	v_mfma_f32_16x16x32_f16 v[94:97], v[144:147], v[128:131], v[94:97]
	v_mfma_f32_16x16x32_f16 v[90:93], v[144:147], v[136:139], v[90:93]
	v_mfma_f32_16x16x32_f16 v[86:89], v[152:155], v[128:131], v[86:89]
	v_mfma_f32_16x16x32_f16 v[82:85], v[152:155], v[136:139], v[82:85]
	v_mfma_f32_16x16x32_f16 v[78:81], v[160:163], v[128:131], v[78:81]
	v_mfma_f32_16x16x32_f16 v[74:77], v[160:163], v[136:139], v[74:77]
	v_mfma_f32_16x16x32_f16 v[94:97], v[148:151], v[132:135], v[94:97]
	v_mfma_f32_16x16x32_f16 v[90:93], v[148:151], v[140:143], v[90:93]
	v_mfma_f32_16x16x32_f16 v[86:89], v[156:159], v[132:135], v[86:89]
	v_mfma_f32_16x16x32_f16 v[82:85], v[156:159], v[140:143], v[82:85]
	v_mfma_f32_16x16x32_f16 v[78:81], v[164:167], v[132:135], v[78:81]
	v_mfma_f32_16x16x32_f16 v[74:77], v[164:167], v[140:143], v[74:77]
	s_setprio 0
	s_barrier
	ds_read_b128 v[168:171], v114
	ds_read_b128 v[172:175], v114 offset:1024
	ds_read_b128 v[176:179], v114 offset:2048
	ds_read_b128 v[180:183], v114 offset:3072
	s_mov_b32 s42, s70
	s_add_u32 s54, s34, s26
	s_addc_u32 s55, s35, s27
	s_mov_b32 m0, s42
	s_nop 0
	global_load_lds_dwordx4 v100, s[54:55]
	s_mov_b32 s42, s71
	s_add_u32 s54, s34, s26
	s_addc_u32 s55, s35, s27
	s_mov_b32 m0, s42
	s_nop 0
	global_load_lds_dwordx4 v103, s[54:55]
	s_barrier
	s_waitcnt lgkmcnt(0)
	s_setprio 1
	s_waitcnt lgkmcnt(0)
	v_mfma_f32_16x16x32_f16 v[70:73], v[144:147], v[168:171], v[70:73]
	v_mfma_f32_16x16x32_f16 v[66:69], v[144:147], v[176:179], v[66:69]
	v_mfma_f32_16x16x32_f16 v[62:65], v[152:155], v[168:171], v[62:65]
	v_mfma_f32_16x16x32_f16 v[50:53], v[152:155], v[176:179], v[50:53]
	v_mfma_f32_16x16x32_f16 v[46:49], v[160:163], v[168:171], v[46:49]
	v_mfma_f32_16x16x32_f16 v[42:45], v[160:163], v[176:179], v[42:45]
	v_mfma_f32_16x16x32_f16 v[70:73], v[148:151], v[172:175], v[70:73]
	v_mfma_f32_16x16x32_f16 v[66:69], v[148:151], v[180:183], v[66:69]
	v_mfma_f32_16x16x32_f16 v[62:65], v[156:159], v[172:175], v[62:65]
	v_mfma_f32_16x16x32_f16 v[50:53], v[156:159], v[180:183], v[50:53]
	v_mfma_f32_16x16x32_f16 v[46:49], v[164:167], v[172:175], v[46:49]
	v_mfma_f32_16x16x32_f16 v[42:45], v[164:167], v[180:183], v[42:45]
	s_setprio 0
	s_barrier
	ds_read_b128 v[144:147], v110 offset:36864
	ds_read_b128 v[148:151], v110 offset:37888
	ds_read_b128 v[152:155], v109 offset:36864
	ds_read_b128 v[156:159], v109 offset:37888
	ds_read_b128 v[160:163], v108 offset:36864
	ds_read_b128 v[164:167], v108 offset:37888
	s_mov_b32 s42, s72
	s_add_u32 s54, s30, s26
	s_addc_u32 s55, s31, s27
	s_mov_b32 m0, s42
	s_nop 0
	global_load_lds_dwordx4 v100, s[54:55]
	s_nop 0
	s_add_u32 s54, s30, s26
	s_addc_u32 s55, s31, s27
	s_mov_b32 s30, s73
	s_mov_b32 m0, s30
	s_nop 0
	global_load_lds_dwordx4 v101, s[54:55]
	s_barrier
	s_waitcnt lgkmcnt(0)
	s_setprio 1
	s_waitcnt lgkmcnt(0)
	v_mfma_f32_16x16x32_f16 v[38:41], v[144:147], v[128:131], v[38:41]
	v_mfma_f32_16x16x32_f16 v[34:37], v[144:147], v[136:139], v[34:37]
	v_mfma_f32_16x16x32_f16 v[30:33], v[152:155], v[128:131], v[30:33]
	v_mfma_f32_16x16x32_f16 v[26:29], v[152:155], v[136:139], v[26:29]
	v_mfma_f32_16x16x32_f16 v[22:25], v[160:163], v[128:131], v[22:25]
	v_mfma_f32_16x16x32_f16 v[18:21], v[160:163], v[136:139], v[18:21]
	v_mfma_f32_16x16x32_f16 v[38:41], v[148:151], v[132:135], v[38:41]
	v_mfma_f32_16x16x32_f16 v[34:37], v[148:151], v[140:143], v[34:37]
	v_mfma_f32_16x16x32_f16 v[30:33], v[156:159], v[132:135], v[30:33]
	v_mfma_f32_16x16x32_f16 v[26:29], v[156:159], v[140:143], v[26:29]
	v_mfma_f32_16x16x32_f16 v[22:25], v[164:167], v[132:135], v[22:25]
	v_mfma_f32_16x16x32_f16 v[18:21], v[164:167], v[140:143], v[18:21]
	s_setprio 0
	s_barrier
	s_mov_b32 s30, s74
	s_add_u32 s56, s34, s28
	s_addc_u32 s57, s35, s29
	s_mov_b32 m0, s30
	s_nop 0
	global_load_lds_dwordx4 v100, s[56:57]
	s_mov_b32 s30, s75
	s_add_u32 s56, s34, s28
	s_addc_u32 s57, s35, s29
	s_mov_b32 m0, s30
	s_nop 0
	global_load_lds_dwordx4 v103, s[56:57]
	s_waitcnt vmcnt(6)
	s_barrier
	s_setprio 1
	v_mfma_f32_16x16x32_f16 v[14:17], v[144:147], v[168:171], v[14:17]
	v_mfma_f32_16x16x32_f16 v[10:13], v[144:147], v[176:179], v[10:13]
	v_mfma_f32_16x16x32_f16 v[6:9], v[152:155], v[168:171], v[6:9]
	v_mfma_f32_16x16x32_f16 v[2:5], v[152:155], v[176:179], v[2:5]
	v_mfma_f32_16x16x32_f16 v[54:57], v[160:163], v[168:171], v[54:57]
	v_mfma_f32_16x16x32_f16 v[58:61], v[160:163], v[176:179], v[58:61]
	v_mfma_f32_16x16x32_f16 v[14:17], v[148:151], v[172:175], v[14:17]
	v_mfma_f32_16x16x32_f16 v[10:13], v[148:151], v[180:183], v[10:13]
	v_mfma_f32_16x16x32_f16 v[6:9], v[156:159], v[172:175], v[6:9]
	v_mfma_f32_16x16x32_f16 v[2:5], v[156:159], v[180:183], v[2:5]
	v_mfma_f32_16x16x32_f16 v[54:57], v[164:167], v[172:175], v[54:57]
	v_mfma_f32_16x16x32_f16 v[58:61], v[164:167], v[180:183], v[58:61]
	s_setprio 0
	s_add_i32 s41, s41, 2
	s_add_u32 s0, s0, 0x100
	s_addc_u32 s1, s1, 0
	s_cmp_lt_u32 s41, 12
	s_barrier
	s_cbranch_scc1 .LBB1_3
	v_add_u32_e32 v98, 0x9000, v1
	s_add_u32 s0, s16, 0x30780
	v_readfirstlane_b32 s2, v98
	s_addc_u32 s1, s17, 0
	s_mov_b32 m0, s2
	v_readfirstlane_b32 s2, v125
	ds_read_b128 v[118:121], v126 offset:49152
	ds_read_b128 v[128:131], v126 offset:50176
	ds_read_b128 v[132:135], v126 offset:51200
	ds_read_b128 v[136:139], v126 offset:52224
	ds_read_b128 v[140:143], v110
	ds_read_b128 v[144:147], v110 offset:1024
	ds_read_b128 v[148:151], v109
	ds_read_b128 v[152:155], v109 offset:1024
	ds_read_b128 v[156:159], v108
	ds_read_b128 v[160:163], v108 offset:1024
	s_nop 0
	global_load_lds_dwordx4 v100, s[0:1]
	s_mov_b32 m0, s2
	s_nop 0
	global_load_lds_dwordx4 v101, s[0:1]
	s_barrier
	s_waitcnt lgkmcnt(0)
	s_setprio 1
	s_waitcnt lgkmcnt(0)
	v_mfma_f32_16x16x32_f16 v[90:93], v[140:143], v[132:135], v[90:93]
	v_mfma_f32_16x16x32_f16 v[86:89], v[148:151], v[118:121], v[86:89]
	v_mfma_f32_16x16x32_f16 v[82:85], v[148:151], v[132:135], v[82:85]
	v_mfma_f32_16x16x32_f16 v[94:97], v[140:143], v[118:121], v[94:97]
	v_mfma_f32_16x16x32_f16 v[90:93], v[144:147], v[136:139], v[90:93]
	v_mfma_f32_16x16x32_f16 v[86:89], v[152:155], v[128:131], v[86:89]
	v_mfma_f32_16x16x32_f16 v[82:85], v[152:155], v[136:139], v[82:85]
	v_mfma_f32_16x16x32_f16 v[78:81], v[156:159], v[118:121], v[78:81]
	v_mfma_f32_16x16x32_f16 v[74:77], v[156:159], v[132:135], v[74:77]
	v_mfma_f32_16x16x32_f16 v[94:97], v[144:147], v[128:131], v[94:97]
	v_mfma_f32_16x16x32_f16 v[124:127], v[160:163], v[128:131], v[78:81]
	v_mfma_f32_16x16x32_f16 v[164:167], v[160:163], v[136:139], v[74:77]
	s_setprio 0
	s_barrier
	s_nop 2
	ds_read_b128 v[74:77], v122
	ds_read_b128 v[78:81], v122 offset:1024
	ds_read_b128 v[98:101], v122 offset:2048
	ds_read_b128 v[168:171], v122 offset:3072
	s_barrier
	s_waitcnt lgkmcnt(0)
	s_setprio 1
	s_waitcnt lgkmcnt(0)
	v_mfma_f32_16x16x32_f16 v[70:73], v[140:143], v[74:77], v[70:73]
	v_mfma_f32_16x16x32_f16 v[66:69], v[140:143], v[98:101], v[66:69]
	v_mfma_f32_16x16x32_f16 v[50:53], v[148:151], v[98:101], v[50:53]
	v_mfma_f32_16x16x32_f16 v[46:49], v[156:159], v[74:77], v[46:49]
	v_mfma_f32_16x16x32_f16 v[42:45], v[156:159], v[98:101], v[42:45]
	v_mfma_f32_16x16x32_f16 v[70:73], v[144:147], v[78:81], v[70:73]
	v_mfma_f32_16x16x32_f16 v[66:69], v[144:147], v[168:171], v[66:69]
	v_mfma_f32_16x16x32_f16 v[62:65], v[148:151], v[74:77], v[62:65]
	v_mfma_f32_16x16x32_f16 v[50:53], v[152:155], v[168:171], v[50:53]
	v_mfma_f32_16x16x32_f16 v[46:49], v[160:163], v[78:81], v[46:49]
	v_mfma_f32_16x16x32_f16 v[42:45], v[160:163], v[168:171], v[42:45]
	v_mfma_f32_16x16x32_f16 v[140:143], v[152:155], v[78:81], v[62:65]
	s_setprio 0
	s_barrier
	s_nop 1
	ds_read_b128 v[62:65], v110 offset:12288
	ds_read_b128 v[144:147], v110 offset:13312
	ds_read_b128 v[148:151], v109 offset:12288
	ds_read_b128 v[152:155], v109 offset:13312
	ds_read_b128 v[156:159], v108 offset:12288
	ds_read_b128 v[160:163], v108 offset:13312
	s_waitcnt vmcnt(4)
	s_barrier
	s_waitcnt lgkmcnt(0)
	s_setprio 1
	s_waitcnt lgkmcnt(0)
	v_mfma_f32_16x16x32_f16 v[38:41], v[62:65], v[118:121], v[38:41]
	v_mfma_f32_16x16x32_f16 v[34:37], v[62:65], v[132:135], v[34:37]
	v_mfma_f32_16x16x32_f16 v[30:33], v[148:151], v[118:121], v[30:33]
	v_mfma_f32_16x16x32_f16 v[26:29], v[148:151], v[132:135], v[26:29]
	v_mfma_f32_16x16x32_f16 v[22:25], v[156:159], v[118:121], v[22:25]
	v_mfma_f32_16x16x32_f16 v[18:21], v[156:159], v[132:135], v[18:21]
	v_mfma_f32_16x16x32_f16 v[38:41], v[144:147], v[128:131], v[38:41]
	v_mfma_f32_16x16x32_f16 v[34:37], v[144:147], v[136:139], v[34:37]
	v_mfma_f32_16x16x32_f16 v[30:33], v[152:155], v[128:131], v[30:33]
	v_mfma_f32_16x16x32_f16 v[26:29], v[152:155], v[136:139], v[26:29]
	v_mfma_f32_16x16x32_f16 v[22:25], v[160:163], v[128:131], v[22:25]
	v_mfma_f32_16x16x32_f16 v[18:21], v[160:163], v[136:139], v[18:21]
	s_setprio 0
	s_setprio 1
	v_mfma_f32_16x16x32_f16 v[10:13], v[62:65], v[98:101], v[10:13]
	v_mfma_f32_16x16x32_f16 v[128:131], v[144:147], v[168:171], v[10:13]
	v_mfma_f32_16x16x32_f16 v[6:9], v[148:151], v[74:77], v[6:9]
	v_mfma_f32_16x16x32_f16 v[2:5], v[148:151], v[98:101], v[2:5]
	v_mfma_f32_16x16x32_f16 v[10:13], v[156:159], v[74:77], v[54:57]
	v_mfma_f32_16x16x32_f16 v[14:17], v[62:65], v[74:77], v[14:17]
	v_mfma_f32_16x16x32_f16 v[6:9], v[152:155], v[78:81], v[6:9]
	v_mfma_f32_16x16x32_f16 v[2:5], v[152:155], v[168:171], v[2:5]
	v_mfma_f32_16x16x32_f16 v[132:135], v[160:163], v[78:81], v[10:13]
	v_mfma_f32_16x16x32_f16 v[10:13], v[156:159], v[98:101], v[58:61]
	v_mfma_f32_16x16x32_f16 v[118:121], v[144:147], v[78:81], v[14:17]
	v_mfma_f32_16x16x32_f16 v[136:139], v[160:163], v[168:171], v[10:13]
	s_setprio 0
	s_barrier
	s_nop 3
	ds_read_b128 v[10:13], v117
	ds_read_b128 v[14:17], v117 offset:1024
	ds_read_b128 v[144:147], v117 offset:2048
	ds_read_b128 v[148:151], v117 offset:3072
	ds_read_b128 v[54:57], v110 offset:24576
	ds_read_b128 v[152:155], v110 offset:25600
	ds_read_b128 v[156:159], v109 offset:24576
	ds_read_b128 v[160:163], v109 offset:25600
	ds_read_b128 v[168:171], v108 offset:24576
	ds_read_b128 v[172:175], v108 offset:25600
	s_waitcnt vmcnt(2)
	s_barrier
	s_waitcnt lgkmcnt(0)
	s_setprio 1
	s_waitcnt lgkmcnt(0)
	v_mfma_f32_16x16x32_f16 v[58:61], v[54:57], v[10:13], v[94:97]
	v_mfma_f32_16x16x32_f16 v[98:101], v[152:155], v[14:17], v[58:61]
	v_mfma_f32_16x16x32_f16 v[58:61], v[54:57], v[144:147], v[90:93]
	v_mfma_f32_16x16x32_f16 v[90:93], v[152:155], v[148:151], v[58:61]
	v_mfma_f32_16x16x32_f16 v[58:61], v[156:159], v[10:13], v[86:89]
	v_mfma_f32_16x16x32_f16 v[78:81], v[160:163], v[14:17], v[58:61]
	v_mfma_f32_16x16x32_f16 v[58:61], v[156:159], v[144:147], v[82:85]
	v_mfma_f32_16x16x32_f16 v[74:77], v[160:163], v[148:151], v[58:61]
	v_mfma_f32_16x16x32_f16 v[58:61], v[168:171], v[10:13], v[124:127]
	v_mfma_f32_16x16x32_f16 v[62:65], v[172:175], v[14:17], v[58:61]
	v_mfma_f32_16x16x32_f16 v[58:61], v[168:171], v[144:147], v[164:167]
	v_mfma_f32_16x16x32_f16 v[58:61], v[172:175], v[148:151], v[58:61]
	s_setprio 0
	s_barrier
	ds_read_b128 v[94:97], v114
	ds_read_b128 v[122:125], v114 offset:1024
	ds_read_b128 v[164:167], v114 offset:2048
	ds_read_b128 v[112:115], v114 offset:3072
	s_waitcnt vmcnt(0)
	s_barrier
	s_waitcnt lgkmcnt(0)
	s_setprio 1
	s_waitcnt lgkmcnt(0)
	v_mfma_f32_16x16x32_f16 v[70:73], v[54:57], v[94:97], v[70:73]
	v_mfma_f32_16x16x32_f16 v[54:57], v[54:57], v[164:167], v[66:69]
	v_mfma_f32_16x16x32_f16 v[82:85], v[152:155], v[112:115], v[54:57]
	v_mfma_f32_16x16x32_f16 v[54:57], v[156:159], v[94:97], v[140:143]
	v_mfma_f32_16x16x32_f16 v[50:53], v[156:159], v[164:167], v[50:53]
	v_mfma_f32_16x16x32_f16 v[46:49], v[168:171], v[94:97], v[46:49]
	v_mfma_f32_16x16x32_f16 v[42:45], v[168:171], v[164:167], v[42:45]
	v_mfma_f32_16x16x32_f16 v[86:89], v[152:155], v[122:125], v[70:73]
	v_mfma_f32_16x16x32_f16 v[70:73], v[160:163], v[122:125], v[54:57]
	v_mfma_f32_16x16x32_f16 v[66:69], v[160:163], v[112:115], v[50:53]
	v_mfma_f32_16x16x32_f16 v[54:57], v[172:175], v[122:125], v[46:49]
	v_mfma_f32_16x16x32_f16 v[50:53], v[172:175], v[112:115], v[42:45]
	s_setprio 0
	s_barrier
	ds_read_b128 v[140:143], v110 offset:36864
	ds_read_b128 v[152:155], v110 offset:37888
	ds_read_b128 v[156:159], v109 offset:36864
	ds_read_b128 v[160:163], v109 offset:37888
	ds_read_b128 v[168:171], v108 offset:36864
	ds_read_b128 v[106:109], v108 offset:37888
	s_barrier
	s_waitcnt lgkmcnt(0)
	s_setprio 1
	s_waitcnt lgkmcnt(0)
	v_mfma_f32_16x16x32_f16 v[38:41], v[140:143], v[10:13], v[38:41]
	v_mfma_f32_16x16x32_f16 v[30:33], v[156:159], v[10:13], v[30:33]
	v_mfma_f32_16x16x32_f16 v[10:13], v[168:171], v[10:13], v[22:25]
	v_mfma_f32_16x16x32_f16 v[46:49], v[152:155], v[14:17], v[38:41]
	v_mfma_f32_16x16x32_f16 v[34:37], v[140:143], v[144:147], v[34:37]
	v_mfma_f32_16x16x32_f16 v[30:33], v[160:163], v[14:17], v[30:33]
	v_mfma_f32_16x16x32_f16 v[26:29], v[156:159], v[144:147], v[26:29]
	v_mfma_f32_16x16x32_f16 v[14:17], v[106:109], v[14:17], v[10:13]
	v_mfma_f32_16x16x32_f16 v[10:13], v[168:171], v[144:147], v[18:21]
	v_mfma_f32_16x16x32_f16 v[42:45], v[152:155], v[148:151], v[34:37]
	v_mfma_f32_16x16x32_f16 v[26:29], v[160:163], v[148:151], v[26:29]
	v_mfma_f32_16x16x32_f16 v[10:13], v[106:109], v[148:151], v[10:13]
	s_setprio 0
	s_setprio 1
	v_mfma_f32_16x16x32_f16 v[18:21], v[140:143], v[94:97], v[118:121]
	v_mfma_f32_16x16x32_f16 v[38:41], v[152:155], v[122:125], v[18:21]
	v_mfma_f32_16x16x32_f16 v[18:21], v[140:143], v[164:167], v[128:131]
	v_mfma_f32_16x16x32_f16 v[2:5], v[156:159], v[164:167], v[2:5]
	v_mfma_f32_16x16x32_f16 v[34:37], v[152:155], v[112:115], v[18:21]
	v_mfma_f32_16x16x32_f16 v[6:9], v[156:159], v[94:97], v[6:9]
	v_mfma_f32_16x16x32_f16 v[18:21], v[160:163], v[112:115], v[2:5]
	v_mfma_f32_16x16x32_f16 v[2:5], v[168:171], v[94:97], v[132:135]
	v_mfma_f32_16x16x32_f16 v[22:25], v[160:163], v[122:125], v[6:9]
	v_mfma_f32_16x16x32_f16 v[6:9], v[106:109], v[122:125], v[2:5]
	v_mfma_f32_16x16x32_f16 v[2:5], v[168:171], v[164:167], v[136:139]
	v_mfma_f32_16x16x32_f16 v[2:5], v[106:109], v[112:115], v[2:5]
	s_setprio 0
	s_andn2_b64 vcc, exec, vcc
	s_barrier
	s_cbranch_vccnz .LBB1_6
	s_barrier
